# attention-output GEMM phase: half of the row panels start about 10 us late so that the HBM-heavy fused epilogues of one half overlap the MFMA K-loops of the other
# baseline (speedup 1.0000x reference)
.LBB0_691:
	s_bitcmp1_b32 s12, 3
	s_cbranch_scc0 .Lp5_nodelay
	s_sleep 127
	s_sleep 127
